# NA window mask P0 part: 16 divergent in-branch LDS reads with lgkmcnt(0) each replaced by hoisted pipelined ds_read + v_cndmask (branch-free), all 5 step copies
# speedup vs baseline: 1.0419x; 1.0419x over previous
.LBB0_534:
	v_mad_u64_u32 v[14:15], s[44:45], s42, v241, v[204:205]
	s_mul_i32 s27, s43, 0x3600
	v_add_u32_e32 v15, s27, v15
	s_add_i32 s27, s47, s9
	s_mov_b32 s42, m0
	s_mov_b32 m0, s27
	s_nop 0
	global_load_lds_dwordx4 v[14:15], off
	s_mov_b32 m0, s42
	s_cmp_lt_u32 s26, 4
	s_cbranch_scc1 .LBB0_568
	s_add_i32 s27, s50, s23
	s_add_i32 s27, s27, -5
	s_cmp_gt_u32 s27, 7
	s_cselect_b64 vcc, -1, 0
	s_add_i32 s27, s49, s23
	s_add_i32 s27, s27, -5
	s_max_i32 s27, s27, -7
	s_add_i32 s27, s27, 7
	s_min_u32 s27, s27, 14
	s_mulk_i32 s27, 0x7c
	v_add_u32_e32 v161, s27, v228
	v_mov_b32_e32 v15, v223
	ds_read_b32 v160, v161 offset:128
	ds_read_b32 v64, v161
	ds_read_b32 v65, v161 offset:4
	ds_read_b32 v66, v161 offset:8
	ds_read_b32 v67, v161 offset:12
	ds_read_b32 v68, v161 offset:32
	ds_read_b32 v69, v161 offset:36
	v_cndmask_b32_e32 v14, 0, v242, vcc
	v_cmp_gt_u32_e32 vcc, 16, v15
	s_waitcnt lgkmcnt(5)
	v_add_f32_e32 v64, v14, v64
	v_add_f32_e32 v64, v112, v64
	v_cndmask_b32_e32 v64, v242, v64, vcc
	ds_read_b32 v70, v161 offset:40
	ds_read_b32 v112, v161 offset:132
	v_add_u32_e32 v162, 1, v15
	v_cmp_gt_u32_e32 vcc, 16, v162
	s_waitcnt lgkmcnt(6)
	v_add_f32_e32 v65, v14, v65
	v_add_f32_e32 v65, v113, v65
	v_cndmask_b32_e32 v65, v242, v65, vcc
	ds_read_b32 v71, v161 offset:44
	ds_read_b32 v113, v161 offset:136
	v_add_u32_e32 v163, 2, v15
	v_cmp_gt_u32_e32 vcc, 16, v163
	s_waitcnt lgkmcnt(7)
	v_add_f32_e32 v66, v14, v66
	v_add_f32_e32 v66, v114, v66
	v_cndmask_b32_e32 v66, v242, v66, vcc
	ds_read_b32 v72, v161 offset:64
	ds_read_b32 v114, v161 offset:140
	v_add_u32_e32 v164, 3, v15
	v_cmp_gt_u32_e32 vcc, 16, v164
	s_waitcnt lgkmcnt(8)
	v_add_f32_e32 v67, v14, v67
	v_add_f32_e32 v67, v115, v67
	v_cndmask_b32_e32 v67, v242, v67, vcc
	ds_read_b32 v73, v161 offset:68
	ds_read_b32 v115, v161 offset:160
	v_add_u32_e32 v165, 8, v15
	v_cmp_gt_u32_e32 vcc, 16, v165
	s_waitcnt lgkmcnt(9)
	v_add_f32_e32 v68, v14, v68
	v_add_f32_e32 v68, v116, v68
	v_cndmask_b32_e32 v68, v242, v68, vcc
	ds_read_b32 v74, v161 offset:72
	ds_read_b32 v116, v161 offset:164
	v_add_u32_e32 v166, 9, v15
	v_cmp_gt_u32_e32 vcc, 16, v166
	s_waitcnt lgkmcnt(10)
	v_add_f32_e32 v69, v14, v69
	v_add_f32_e32 v69, v117, v69
	v_cndmask_b32_e32 v69, v242, v69, vcc
	ds_read_b32 v75, v161 offset:76
	ds_read_b32 v117, v161 offset:168
	v_add_u32_e32 v167, 10, v15
	v_cmp_gt_u32_e32 vcc, 16, v167
	s_waitcnt lgkmcnt(11)
	v_add_f32_e32 v70, v14, v70
	v_add_f32_e32 v70, v118, v70
	v_cndmask_b32_e32 v70, v242, v70, vcc
	ds_read_b32 v76, v161 offset:96
	ds_read_b32 v118, v161 offset:172
	v_add_u32_e32 v168, 11, v15
	v_cmp_gt_u32_e32 vcc, 16, v168
	s_waitcnt lgkmcnt(11)
	v_add_f32_e32 v71, v14, v71
	v_add_f32_e32 v71, v119, v71
	v_cndmask_b32_e32 v71, v242, v71, vcc
	ds_read_b32 v77, v161 offset:100
	ds_read_b32 v119, v161 offset:192
	v_cmp_lt_u32_e32 vcc, s79, v15
	s_waitcnt lgkmcnt(11)
	v_add_f32_e32 v72, v14, v72
	v_add_f32_e32 v72, v120, v72
	v_cndmask_b32_e32 v72, v242, v72, vcc
	ds_read_b32 v78, v161 offset:104
	ds_read_b32 v120, v161 offset:196
	v_add_u32_e32 v169, 17, v15
	v_cmp_gt_u32_e32 vcc, 16, v169
	s_waitcnt lgkmcnt(11)
	v_add_f32_e32 v73, v14, v73
	v_add_f32_e32 v73, v121, v73
	v_cndmask_b32_e32 v73, v242, v73, vcc
	ds_read_b32 v79, v161 offset:108
	ds_read_b32 v121, v161 offset:200
	v_add_u32_e32 v170, 18, v15
	v_cmp_gt_u32_e32 vcc, 16, v170
	s_waitcnt lgkmcnt(11)
	v_add_f32_e32 v74, v14, v74
	v_add_f32_e32 v74, v122, v74
	v_cndmask_b32_e32 v74, v242, v74, vcc
	ds_read_b32 v122, v161 offset:204
	v_add_u32_e32 v171, 19, v15
	v_cmp_gt_u32_e32 vcc, 16, v171
	s_waitcnt lgkmcnt(10)
	v_add_f32_e32 v75, v14, v75
	v_add_f32_e32 v75, v123, v75
	v_cndmask_b32_e32 v75, v242, v75, vcc
	ds_read_b32 v123, v161 offset:224
	v_add_u32_e32 v172, 24, v15
	v_cmp_gt_u32_e32 vcc, 16, v172
	s_waitcnt lgkmcnt(9)
	v_add_f32_e32 v76, v14, v76
	v_add_f32_e32 v76, v124, v76
	v_cndmask_b32_e32 v76, v242, v76, vcc
	ds_read_b32 v124, v161 offset:228
	v_add_u32_e32 v173, 25, v15
	v_cmp_gt_u32_e32 vcc, 16, v173
	s_waitcnt lgkmcnt(8)
	v_add_f32_e32 v77, v14, v77
	v_add_f32_e32 v77, v125, v77
	v_cndmask_b32_e32 v77, v242, v77, vcc
	ds_read_b32 v174, v161 offset:232
	v_add_u32_e32 v175, 26, v15
	v_cmp_gt_u32_e32 vcc, 16, v175
	s_waitcnt lgkmcnt(7)
	v_add_f32_e32 v78, v14, v78
	v_add_f32_e32 v78, v126, v78
	v_cndmask_b32_e32 v78, v242, v78, vcc
	ds_read_b32 v126, v161 offset:236
	v_add_u32_e32 v125, 27, v15
	v_cmp_gt_u32_e32 vcc, 16, v125
	s_waitcnt lgkmcnt(6)
	v_add_f32_e32 v79, v14, v79
	v_add_f32_e32 v79, v127, v79
	v_cndmask_b32_e32 v79, v242, v79, vcc
	s_waitcnt lgkmcnt(14)
	v_add_f32_e32 v127, v14, v160
	v_and_b32_e32 v15, -16, v15
	v_add_f32_e32 v96, v96, v127
	v_cmp_eq_u32_e32 vcc, s76, v15
	v_add_f32_e32 v112, v14, v112
	v_and_b32_e32 v127, -16, v162
	v_cndmask_b32_e32 v96, v242, v96, vcc
	v_add_f32_e32 v97, v97, v112
	v_cmp_eq_u32_e32 vcc, s76, v127
	s_waitcnt lgkmcnt(13)
	v_add_f32_e32 v112, v14, v113
	v_and_b32_e32 v113, -16, v163
	v_cndmask_b32_e32 v97, v242, v97, vcc
	v_add_f32_e32 v98, v98, v112
	v_cmp_eq_u32_e32 vcc, s76, v113
	s_waitcnt lgkmcnt(12)
	v_add_f32_e32 v112, v14, v114
	v_and_b32_e32 v113, -16, v164
	v_cndmask_b32_e32 v98, v242, v98, vcc
	v_add_f32_e32 v99, v99, v112
	v_cmp_eq_u32_e32 vcc, s76, v113
	s_waitcnt lgkmcnt(11)
	v_add_f32_e32 v112, v14, v115
	v_and_b32_e32 v113, -16, v165
	v_cndmask_b32_e32 v99, v242, v99, vcc
	v_add_f32_e32 v100, v100, v112
	v_cmp_eq_u32_e32 vcc, s76, v113
	s_waitcnt lgkmcnt(10)
	v_add_f32_e32 v112, v14, v116
	v_and_b32_e32 v113, -16, v166
	v_cndmask_b32_e32 v100, v242, v100, vcc
	v_add_f32_e32 v101, v101, v112
	v_cmp_eq_u32_e32 vcc, s76, v113
	s_waitcnt lgkmcnt(9)
	v_add_f32_e32 v112, v14, v117
	v_and_b32_e32 v113, -16, v167
	v_cndmask_b32_e32 v101, v242, v101, vcc
	v_add_f32_e32 v102, v102, v112
	v_cmp_eq_u32_e32 vcc, s76, v113
	s_waitcnt lgkmcnt(8)
	v_add_f32_e32 v112, v14, v118
	v_and_b32_e32 v113, -16, v168
	v_cndmask_b32_e32 v102, v242, v102, vcc
	v_add_f32_e32 v103, v103, v112
	v_cmp_eq_u32_e32 vcc, s76, v113
	s_waitcnt lgkmcnt(7)
	v_add_f32_e32 v112, v14, v119
	v_add_f32_e32 v104, v104, v112
	v_cndmask_b32_e32 v103, v242, v103, vcc
	v_cmp_eq_u32_e32 vcc, s78, v15
	s_waitcnt lgkmcnt(6)
	v_add_f32_e32 v15, v14, v120
	v_and_b32_e32 v112, -16, v169
	v_cndmask_b32_e32 v104, v242, v104, vcc
	v_add_f32_e32 v15, v105, v15
	v_cmp_eq_u32_e32 vcc, s76, v112
	v_and_b32_e32 v112, -16, v170
	s_nop 0
	v_cndmask_b32_e32 v105, v242, v15, vcc
	s_waitcnt lgkmcnt(5)
	v_add_f32_e32 v15, v14, v121
	v_add_f32_e32 v15, v106, v15
	v_cmp_eq_u32_e32 vcc, s76, v112
	v_and_b32_e32 v112, -16, v171
	s_nop 0
	v_cndmask_b32_e32 v106, v242, v15, vcc
	s_waitcnt lgkmcnt(4)
	v_add_f32_e32 v15, v14, v122
	v_add_f32_e32 v15, v107, v15
	v_cmp_eq_u32_e32 vcc, s76, v112
	v_and_b32_e32 v112, -16, v172
	s_nop 0
	v_cndmask_b32_e32 v107, v242, v15, vcc
	s_waitcnt lgkmcnt(3)
	v_add_f32_e32 v15, v14, v123
	v_add_f32_e32 v15, v108, v15
	v_cmp_eq_u32_e32 vcc, s76, v112
	v_and_b32_e32 v112, -16, v173
	s_nop 0
	v_cndmask_b32_e32 v108, v242, v15, vcc
	s_waitcnt lgkmcnt(2)
	v_add_f32_e32 v15, v14, v124
	v_add_f32_e32 v15, v109, v15
	v_cmp_eq_u32_e32 vcc, s76, v112
	v_and_b32_e32 v112, -16, v175
	s_nop 0
	v_cndmask_b32_e32 v109, v242, v15, vcc
	s_waitcnt lgkmcnt(1)
	v_add_f32_e32 v15, v14, v174
	v_add_f32_e32 v15, v110, v15
	v_cmp_eq_u32_e32 vcc, s76, v112
	s_waitcnt lgkmcnt(0)
	v_add_f32_e32 v14, v14, v126
	v_add_f32_e32 v14, v111, v14
	v_cndmask_b32_e32 v110, v242, v15, vcc
	v_and_b32_e32 v15, -16, v125
	v_cmp_eq_u32_e32 vcc, s76, v15
	v_mov_b64_e32 v[126:127], v[78:79]
	v_mov_b64_e32 v[124:125], v[76:77]
	v_cndmask_b32_e32 v111, v242, v14, vcc
	v_mov_b64_e32 v[122:123], v[74:75]
	v_mov_b64_e32 v[120:121], v[72:73]
	v_mov_b64_e32 v[118:119], v[70:71]
	v_mov_b64_e32 v[116:117], v[68:69]
	v_mov_b64_e32 v[114:115], v[66:67]
	v_mov_b64_e32 v[112:113], v[64:65]

.LBB0_573:
	s_add_i32 s27, s47, 0x2000
	s_cmpk_lg_i32 s47, 0x4000
	s_cselect_b32 s64, s27, 0
	v_mad_u64_u32 v[96:97], s[44:45], s42, v241, v[204:205]
	s_mul_i32 s27, s43, 0x3600
	v_add_u32_e32 v97, s27, v97
	s_add_i32 s27, s64, s9
	s_cmp_lt_u32 s26, 3
	s_mov_b32 s26, m0
	s_mov_b32 m0, s27
	s_nop 0
	global_load_lds_dwordx4 v[96:97], off
	s_mov_b32 m0, s26
	s_cbranch_scc1 .LBB0_607
	s_add_i32 s26, s50, s23
	s_add_i32 s26, s26, -4
	s_cmp_gt_u32 s26, 7
	s_cselect_b64 vcc, -1, 0
	s_add_i32 s26, s49, s23
	s_add_i32 s26, s26, -4
	s_max_i32 s26, s26, -7
	s_add_i32 s26, s26, 7
	s_min_u32 s26, s26, 14
	s_mulk_i32 s26, 0x7c
	v_add_u32_e32 v166, s26, v228
	v_mov_b32_e32 v164, v223
	ds_read_b32 v165, v166 offset:128
	ds_read_b32 v96, v166
	ds_read_b32 v97, v166 offset:4
	ds_read_b32 v98, v166 offset:8
	ds_read_b32 v99, v166 offset:12
	ds_read_b32 v100, v166 offset:32
	ds_read_b32 v101, v166 offset:36
	v_cndmask_b32_e32 v15, 0, v242, vcc
	v_cmp_gt_u32_e32 vcc, 16, v164
	s_waitcnt lgkmcnt(5)
	v_add_f32_e32 v96, v15, v96
	v_add_f32_e32 v96, v80, v96
	v_cndmask_b32_e32 v96, v242, v96, vcc
	ds_read_b32 v102, v166 offset:40
	ds_read_b32 v80, v166 offset:132
	v_add_u32_e32 v167, 1, v164
	v_cmp_gt_u32_e32 vcc, 16, v167
	s_waitcnt lgkmcnt(6)
	v_add_f32_e32 v97, v15, v97
	v_add_f32_e32 v97, v81, v97
	v_cndmask_b32_e32 v97, v242, v97, vcc
	ds_read_b32 v103, v166 offset:44
	ds_read_b32 v81, v166 offset:136
	v_add_u32_e32 v168, 2, v164
	v_cmp_gt_u32_e32 vcc, 16, v168
	s_waitcnt lgkmcnt(7)
	v_add_f32_e32 v98, v15, v98
	v_add_f32_e32 v98, v82, v98
	v_cndmask_b32_e32 v98, v242, v98, vcc
	ds_read_b32 v104, v166 offset:64
	ds_read_b32 v82, v166 offset:140
	v_add_u32_e32 v169, 3, v164
	v_cmp_gt_u32_e32 vcc, 16, v169
	s_waitcnt lgkmcnt(8)
	v_add_f32_e32 v99, v15, v99
	v_add_f32_e32 v99, v83, v99
	v_cndmask_b32_e32 v99, v242, v99, vcc
	ds_read_b32 v105, v166 offset:68
	ds_read_b32 v83, v166 offset:160
	v_add_u32_e32 v170, 8, v164
	v_cmp_gt_u32_e32 vcc, 16, v170
	s_waitcnt lgkmcnt(9)
	v_add_f32_e32 v100, v15, v100
	v_add_f32_e32 v100, v84, v100
	v_cndmask_b32_e32 v100, v242, v100, vcc
	ds_read_b32 v106, v166 offset:72
	ds_read_b32 v84, v166 offset:164
	v_add_u32_e32 v171, 9, v164
	v_cmp_gt_u32_e32 vcc, 16, v171
	s_waitcnt lgkmcnt(10)
	v_add_f32_e32 v101, v15, v101
	v_add_f32_e32 v101, v85, v101
	v_cndmask_b32_e32 v101, v242, v101, vcc
	ds_read_b32 v107, v166 offset:76
	ds_read_b32 v85, v166 offset:168
	v_add_u32_e32 v172, 10, v164
	v_cmp_gt_u32_e32 vcc, 16, v172
	s_waitcnt lgkmcnt(11)
	v_add_f32_e32 v102, v15, v102
	v_add_f32_e32 v102, v86, v102
	v_cndmask_b32_e32 v102, v242, v102, vcc
	ds_read_b32 v108, v166 offset:96
	ds_read_b32 v86, v166 offset:172
	v_add_u32_e32 v173, 11, v164
	v_cmp_gt_u32_e32 vcc, 16, v173
	s_waitcnt lgkmcnt(11)
	v_add_f32_e32 v103, v15, v103
	v_add_f32_e32 v103, v87, v103
	v_cndmask_b32_e32 v103, v242, v103, vcc
	ds_read_b32 v109, v166 offset:100
	ds_read_b32 v87, v166 offset:192
	v_cmp_lt_u32_e32 vcc, s79, v164
	s_waitcnt lgkmcnt(11)
	v_add_f32_e32 v104, v15, v104
	v_add_f32_e32 v104, v88, v104
	v_cndmask_b32_e32 v104, v242, v104, vcc
	ds_read_b32 v110, v166 offset:104
	ds_read_b32 v88, v166 offset:196
	v_add_u32_e32 v174, 17, v164
	v_cmp_gt_u32_e32 vcc, 16, v174
	s_waitcnt lgkmcnt(11)
	v_add_f32_e32 v105, v15, v105
	v_add_f32_e32 v105, v89, v105
	v_cndmask_b32_e32 v105, v242, v105, vcc
	ds_read_b32 v111, v166 offset:108
	ds_read_b32 v89, v166 offset:200
	v_add_u32_e32 v175, 18, v164
	v_cmp_gt_u32_e32 vcc, 16, v175
	s_waitcnt lgkmcnt(11)
	v_add_f32_e32 v106, v15, v106
	v_add_f32_e32 v106, v90, v106
	v_cndmask_b32_e32 v106, v242, v106, vcc
	ds_read_b32 v90, v166 offset:204
	v_add_u32_e32 v176, 19, v164
	v_cmp_gt_u32_e32 vcc, 16, v176
	s_waitcnt lgkmcnt(10)
	v_add_f32_e32 v107, v15, v107
	v_add_f32_e32 v107, v91, v107
	v_cndmask_b32_e32 v107, v242, v107, vcc
	ds_read_b32 v91, v166 offset:224
	v_add_u32_e32 v177, 24, v164
	v_cmp_gt_u32_e32 vcc, 16, v177
	s_waitcnt lgkmcnt(9)
	v_add_f32_e32 v108, v15, v108
	v_add_f32_e32 v108, v92, v108
	v_cndmask_b32_e32 v108, v242, v108, vcc
	ds_read_b32 v92, v166 offset:228
	v_add_u32_e32 v178, 25, v164
	v_cmp_gt_u32_e32 vcc, 16, v178
	s_waitcnt lgkmcnt(8)
	v_add_f32_e32 v109, v15, v109
	v_add_f32_e32 v109, v93, v109
	v_cndmask_b32_e32 v109, v242, v109, vcc
	ds_read_b32 v179, v166 offset:232
	v_add_u32_e32 v180, 26, v164
	v_cmp_gt_u32_e32 vcc, 16, v180
	s_waitcnt lgkmcnt(7)
	v_add_f32_e32 v110, v15, v110
	v_add_f32_e32 v110, v94, v110
	v_cndmask_b32_e32 v110, v242, v110, vcc
	ds_read_b32 v94, v166 offset:236
	v_add_u32_e32 v93, 27, v164
	v_cmp_gt_u32_e32 vcc, 16, v93
	s_waitcnt lgkmcnt(6)
	v_add_f32_e32 v111, v15, v111
	v_add_f32_e32 v111, v95, v111
	v_cndmask_b32_e32 v111, v242, v111, vcc
	s_waitcnt lgkmcnt(14)
	v_add_f32_e32 v95, v15, v165
	v_and_b32_e32 v164, -16, v164
	v_add_f32_e32 v64, v64, v95
	v_cmp_eq_u32_e32 vcc, s76, v164
	v_add_f32_e32 v80, v15, v80
	v_and_b32_e32 v95, -16, v167
	v_cndmask_b32_e32 v64, v242, v64, vcc
	v_add_f32_e32 v65, v65, v80
	v_cmp_eq_u32_e32 vcc, s76, v95
	s_waitcnt lgkmcnt(13)
	v_add_f32_e32 v80, v15, v81
	v_and_b32_e32 v81, -16, v168
	v_cndmask_b32_e32 v65, v242, v65, vcc
	v_add_f32_e32 v66, v66, v80
	v_cmp_eq_u32_e32 vcc, s76, v81
	s_waitcnt lgkmcnt(12)
	v_add_f32_e32 v80, v15, v82
	v_and_b32_e32 v81, -16, v169
	v_cndmask_b32_e32 v66, v242, v66, vcc
	v_add_f32_e32 v67, v67, v80
	v_cmp_eq_u32_e32 vcc, s76, v81
	s_waitcnt lgkmcnt(11)
	v_add_f32_e32 v80, v15, v83
	v_and_b32_e32 v81, -16, v170
	v_cndmask_b32_e32 v67, v242, v67, vcc
	v_add_f32_e32 v68, v68, v80
	v_cmp_eq_u32_e32 vcc, s76, v81
	s_waitcnt lgkmcnt(10)
	v_add_f32_e32 v80, v15, v84
	v_and_b32_e32 v81, -16, v171
	v_cndmask_b32_e32 v68, v242, v68, vcc
	v_add_f32_e32 v69, v69, v80
	v_cmp_eq_u32_e32 vcc, s76, v81
	s_waitcnt lgkmcnt(9)
	v_add_f32_e32 v80, v15, v85
	v_and_b32_e32 v81, -16, v172
	v_cndmask_b32_e32 v69, v242, v69, vcc
	v_add_f32_e32 v70, v70, v80
	v_cmp_eq_u32_e32 vcc, s76, v81
	s_waitcnt lgkmcnt(8)
	v_add_f32_e32 v80, v15, v86
	v_and_b32_e32 v81, -16, v173
	v_cndmask_b32_e32 v70, v242, v70, vcc
	v_add_f32_e32 v71, v71, v80
	v_cmp_eq_u32_e32 vcc, s76, v81
	s_waitcnt lgkmcnt(7)
	v_add_f32_e32 v80, v15, v87
	v_add_f32_e32 v72, v72, v80
	v_cndmask_b32_e32 v71, v242, v71, vcc
	v_cmp_eq_u32_e32 vcc, s78, v164
	s_waitcnt lgkmcnt(6)
	v_add_f32_e32 v80, v15, v88
	v_and_b32_e32 v81, -16, v174
	v_cndmask_b32_e32 v72, v242, v72, vcc
	v_add_f32_e32 v73, v73, v80
	v_cmp_eq_u32_e32 vcc, s76, v81
	s_waitcnt lgkmcnt(5)
	v_add_f32_e32 v80, v15, v89
	v_and_b32_e32 v81, -16, v175
	v_cndmask_b32_e32 v73, v242, v73, vcc
	v_add_f32_e32 v74, v74, v80
	v_cmp_eq_u32_e32 vcc, s76, v81
	s_waitcnt lgkmcnt(4)
	v_add_f32_e32 v80, v15, v90
	v_and_b32_e32 v81, -16, v176
	v_cndmask_b32_e32 v74, v242, v74, vcc
	v_add_f32_e32 v75, v75, v80
	v_cmp_eq_u32_e32 vcc, s76, v81
	s_waitcnt lgkmcnt(3)
	v_add_f32_e32 v80, v15, v91
	v_and_b32_e32 v81, -16, v177
	v_cndmask_b32_e32 v75, v242, v75, vcc
	v_add_f32_e32 v76, v76, v80
	v_cmp_eq_u32_e32 vcc, s76, v81
	s_waitcnt lgkmcnt(2)
	v_add_f32_e32 v80, v15, v92
	v_and_b32_e32 v81, -16, v178
	v_cndmask_b32_e32 v76, v242, v76, vcc
	v_add_f32_e32 v77, v77, v80
	v_cmp_eq_u32_e32 vcc, s76, v81
	s_waitcnt lgkmcnt(1)
	v_add_f32_e32 v80, v15, v179
	v_and_b32_e32 v81, -16, v180
	v_cndmask_b32_e32 v77, v242, v77, vcc
	v_add_f32_e32 v78, v78, v80
	v_cmp_eq_u32_e32 vcc, s76, v81
	s_waitcnt lgkmcnt(0)
	v_add_f32_e32 v15, v15, v94
	v_and_b32_e32 v80, -16, v93
	v_cndmask_b32_e32 v78, v242, v78, vcc
	v_add_f32_e32 v15, v79, v15
	v_cmp_eq_u32_e32 vcc, s76, v80
	v_mov_b64_e32 v[80:81], v[96:97]
	v_mov_b64_e32 v[82:83], v[98:99]
	v_cndmask_b32_e32 v79, v242, v15, vcc
	v_mov_b64_e32 v[84:85], v[100:101]
	v_mov_b64_e32 v[86:87], v[102:103]
	v_mov_b64_e32 v[88:89], v[104:105]
	v_mov_b64_e32 v[90:91], v[106:107]
	v_mov_b64_e32 v[92:93], v[108:109]
	v_mov_b64_e32 v[94:95], v[110:111]

.LBB0_625:
	v_mad_u64_u32 v[64:65], s[46:47], s6, v241, v[204:205]
	s_mul_i32 s6, s7, 0x3600
	v_add_u32_e32 v65, s6, v65
	s_add_i32 s6, s81, s9
	s_mov_b32 s7, m0
	s_mov_b32 m0, s6
	s_nop 0
	global_load_lds_dwordx4 v[64:65], off
	s_mov_b32 m0, s7
	s_cmp_lt_u32 s50, 4
	s_cbranch_scc1 .LBB0_659
	s_add_i32 s6, s23, s90
	s_add_i32 s6, s6, -8
	s_cmp_gt_u32 s6, 7
	s_cselect_b64 vcc, -1, 0
	s_add_i32 s6, s23, s74
	s_max_i32 s6, s6, -7
	s_add_i32 s6, s6, 7
	s_min_u32 s6, s6, 14
	s_mulk_i32 s6, 0x7c
	v_add_u32_e32 v163, s6, v228
	v_mov_b32_e32 v161, v223
	ds_read_b32 v162, v163 offset:128
	ds_read_b32 v64, v163
	ds_read_b32 v65, v163 offset:4
	ds_read_b32 v66, v163 offset:8
	ds_read_b32 v67, v163 offset:12
	ds_read_b32 v68, v163 offset:32
	ds_read_b32 v69, v163 offset:36
	v_cndmask_b32_e32 v160, 0, v242, vcc
	v_cmp_gt_u32_e32 vcc, 16, v161
	s_waitcnt lgkmcnt(5)
	v_add_f32_e32 v64, v160, v64
	v_add_f32_e32 v64, v112, v64
	v_cndmask_b32_e32 v64, v242, v64, vcc
	ds_read_b32 v70, v163 offset:40
	ds_read_b32 v112, v163 offset:132
	v_add_u32_e32 v164, 1, v161
	v_cmp_gt_u32_e32 vcc, 16, v164
	s_waitcnt lgkmcnt(6)
	v_add_f32_e32 v65, v160, v65
	v_add_f32_e32 v65, v113, v65
	v_cndmask_b32_e32 v65, v242, v65, vcc
	ds_read_b32 v71, v163 offset:44
	ds_read_b32 v113, v163 offset:136
	v_add_u32_e32 v165, 2, v161
	v_cmp_gt_u32_e32 vcc, 16, v165
	s_waitcnt lgkmcnt(7)
	v_add_f32_e32 v66, v160, v66
	v_add_f32_e32 v66, v114, v66
	v_cndmask_b32_e32 v66, v242, v66, vcc
	ds_read_b32 v72, v163 offset:64
	ds_read_b32 v114, v163 offset:140
	v_add_u32_e32 v166, 3, v161
	v_cmp_gt_u32_e32 vcc, 16, v166
	s_waitcnt lgkmcnt(8)
	v_add_f32_e32 v67, v160, v67
	v_add_f32_e32 v67, v115, v67
	v_cndmask_b32_e32 v67, v242, v67, vcc
	ds_read_b32 v73, v163 offset:68
	ds_read_b32 v115, v163 offset:160
	v_add_u32_e32 v167, 8, v161
	v_cmp_gt_u32_e32 vcc, 16, v167
	s_waitcnt lgkmcnt(9)
	v_add_f32_e32 v68, v160, v68
	v_add_f32_e32 v68, v116, v68
	v_cndmask_b32_e32 v68, v242, v68, vcc
	ds_read_b32 v74, v163 offset:72
	ds_read_b32 v116, v163 offset:164
	v_add_u32_e32 v168, 9, v161
	v_cmp_gt_u32_e32 vcc, 16, v168
	s_waitcnt lgkmcnt(10)
	v_add_f32_e32 v69, v160, v69
	v_add_f32_e32 v69, v117, v69
	v_cndmask_b32_e32 v69, v242, v69, vcc
	ds_read_b32 v75, v163 offset:76
	ds_read_b32 v117, v163 offset:168
	v_add_u32_e32 v169, 10, v161
	v_cmp_gt_u32_e32 vcc, 16, v169
	s_waitcnt lgkmcnt(11)
	v_add_f32_e32 v70, v160, v70
	v_add_f32_e32 v70, v118, v70
	v_cndmask_b32_e32 v70, v242, v70, vcc
	ds_read_b32 v76, v163 offset:96
	ds_read_b32 v118, v163 offset:172
	v_add_u32_e32 v170, 11, v161
	v_cmp_gt_u32_e32 vcc, 16, v170
	s_waitcnt lgkmcnt(11)
	v_add_f32_e32 v71, v160, v71
	v_add_f32_e32 v71, v119, v71
	v_cndmask_b32_e32 v71, v242, v71, vcc
	ds_read_b32 v77, v163 offset:100
	ds_read_b32 v119, v163 offset:192
	v_cmp_lt_u32_e32 vcc, s79, v161
	s_waitcnt lgkmcnt(11)
	v_add_f32_e32 v72, v160, v72
	v_add_f32_e32 v72, v120, v72
	v_cndmask_b32_e32 v72, v242, v72, vcc
	ds_read_b32 v78, v163 offset:104
	ds_read_b32 v120, v163 offset:196
	v_add_u32_e32 v171, 17, v161
	v_cmp_gt_u32_e32 vcc, 16, v171
	s_waitcnt lgkmcnt(11)
	v_add_f32_e32 v73, v160, v73
	v_add_f32_e32 v73, v121, v73
	v_cndmask_b32_e32 v73, v242, v73, vcc
	ds_read_b32 v79, v163 offset:108
	ds_read_b32 v121, v163 offset:200
	v_add_u32_e32 v172, 18, v161
	v_cmp_gt_u32_e32 vcc, 16, v172
	s_waitcnt lgkmcnt(11)
	v_add_f32_e32 v74, v160, v74
	v_add_f32_e32 v74, v122, v74
	v_cndmask_b32_e32 v74, v242, v74, vcc
	ds_read_b32 v122, v163 offset:204
	v_add_u32_e32 v173, 19, v161
	v_cmp_gt_u32_e32 vcc, 16, v173
	s_waitcnt lgkmcnt(10)
	v_add_f32_e32 v75, v160, v75
	v_add_f32_e32 v75, v123, v75
	v_cndmask_b32_e32 v75, v242, v75, vcc
	ds_read_b32 v123, v163 offset:224
	v_add_u32_e32 v174, 24, v161
	v_cmp_gt_u32_e32 vcc, 16, v174
	s_waitcnt lgkmcnt(9)
	v_add_f32_e32 v76, v160, v76
	v_add_f32_e32 v76, v124, v76
	v_cndmask_b32_e32 v76, v242, v76, vcc
	ds_read_b32 v124, v163 offset:228
	v_add_u32_e32 v175, 25, v161
	v_cmp_gt_u32_e32 vcc, 16, v175
	s_waitcnt lgkmcnt(8)
	v_add_f32_e32 v77, v160, v77
	v_add_f32_e32 v77, v125, v77
	v_cndmask_b32_e32 v77, v242, v77, vcc
	ds_read_b32 v176, v163 offset:232
	v_add_u32_e32 v177, 26, v161
	v_cmp_gt_u32_e32 vcc, 16, v177
	s_waitcnt lgkmcnt(7)
	v_add_f32_e32 v78, v160, v78
	v_add_f32_e32 v78, v126, v78
	v_cndmask_b32_e32 v78, v242, v78, vcc
	ds_read_b32 v126, v163 offset:236
	v_add_u32_e32 v125, 27, v161
	v_cmp_gt_u32_e32 vcc, 16, v125
	s_waitcnt lgkmcnt(6)
	v_add_f32_e32 v79, v160, v79
	v_add_f32_e32 v79, v127, v79
	v_cndmask_b32_e32 v79, v242, v79, vcc
	s_waitcnt lgkmcnt(14)
	v_add_f32_e32 v127, v160, v162
	v_and_b32_e32 v161, -16, v161
	v_add_f32_e32 v96, v96, v127
	v_cmp_eq_u32_e32 vcc, s76, v161
	v_add_f32_e32 v112, v160, v112
	v_and_b32_e32 v127, -16, v164
	v_cndmask_b32_e32 v96, v242, v96, vcc
	v_add_f32_e32 v97, v97, v112
	v_cmp_eq_u32_e32 vcc, s76, v127
	s_waitcnt lgkmcnt(13)
	v_add_f32_e32 v112, v160, v113
	v_and_b32_e32 v113, -16, v165
	v_cndmask_b32_e32 v97, v242, v97, vcc
	v_add_f32_e32 v98, v98, v112
	v_cmp_eq_u32_e32 vcc, s76, v113
	s_waitcnt lgkmcnt(12)
	v_add_f32_e32 v112, v160, v114
	v_and_b32_e32 v113, -16, v166
	v_cndmask_b32_e32 v98, v242, v98, vcc
	v_add_f32_e32 v99, v99, v112
	v_cmp_eq_u32_e32 vcc, s76, v113
	s_waitcnt lgkmcnt(11)
	v_add_f32_e32 v112, v160, v115
	v_and_b32_e32 v113, -16, v167
	v_cndmask_b32_e32 v99, v242, v99, vcc
	v_add_f32_e32 v100, v100, v112
	v_cmp_eq_u32_e32 vcc, s76, v113
	s_waitcnt lgkmcnt(10)
	v_add_f32_e32 v112, v160, v116
	v_and_b32_e32 v113, -16, v168
	v_cndmask_b32_e32 v100, v242, v100, vcc
	v_add_f32_e32 v101, v101, v112
	v_cmp_eq_u32_e32 vcc, s76, v113
	s_waitcnt lgkmcnt(9)
	v_add_f32_e32 v112, v160, v117
	v_and_b32_e32 v113, -16, v169
	v_cndmask_b32_e32 v101, v242, v101, vcc
	v_add_f32_e32 v102, v102, v112
	v_cmp_eq_u32_e32 vcc, s76, v113
	s_waitcnt lgkmcnt(8)
	v_add_f32_e32 v112, v160, v118
	v_and_b32_e32 v113, -16, v170
	v_cndmask_b32_e32 v102, v242, v102, vcc
	v_add_f32_e32 v103, v103, v112
	v_cmp_eq_u32_e32 vcc, s76, v113
	s_waitcnt lgkmcnt(7)
	v_add_f32_e32 v112, v160, v119
	v_add_f32_e32 v104, v104, v112
	v_cndmask_b32_e32 v103, v242, v103, vcc
	v_cmp_eq_u32_e32 vcc, s78, v161
	s_waitcnt lgkmcnt(6)
	v_add_f32_e32 v112, v160, v120
	v_and_b32_e32 v113, -16, v171
	v_cndmask_b32_e32 v104, v242, v104, vcc
	v_add_f32_e32 v105, v105, v112
	v_cmp_eq_u32_e32 vcc, s76, v113
	s_waitcnt lgkmcnt(5)
	v_add_f32_e32 v112, v160, v121
	v_and_b32_e32 v113, -16, v172
	v_cndmask_b32_e32 v105, v242, v105, vcc
	v_add_f32_e32 v106, v106, v112
	v_cmp_eq_u32_e32 vcc, s76, v113
	s_waitcnt lgkmcnt(4)
	v_add_f32_e32 v112, v160, v122
	v_and_b32_e32 v113, -16, v173
	v_cndmask_b32_e32 v106, v242, v106, vcc
	v_add_f32_e32 v107, v107, v112
	v_cmp_eq_u32_e32 vcc, s76, v113
	s_waitcnt lgkmcnt(3)
	v_add_f32_e32 v112, v160, v123
	v_and_b32_e32 v113, -16, v174
	v_cndmask_b32_e32 v107, v242, v107, vcc
	v_add_f32_e32 v108, v108, v112
	v_cmp_eq_u32_e32 vcc, s76, v113
	s_waitcnt lgkmcnt(2)
	v_add_f32_e32 v112, v160, v124
	v_and_b32_e32 v113, -16, v175
	v_cndmask_b32_e32 v108, v242, v108, vcc
	v_add_f32_e32 v109, v109, v112
	v_cmp_eq_u32_e32 vcc, s76, v113
	s_waitcnt lgkmcnt(1)
	v_add_f32_e32 v112, v160, v176
	v_and_b32_e32 v113, -16, v177
	v_cndmask_b32_e32 v109, v242, v109, vcc
	v_add_f32_e32 v110, v110, v112
	v_cmp_eq_u32_e32 vcc, s76, v113
	s_waitcnt lgkmcnt(0)
	v_add_f32_e32 v112, v160, v126
	v_and_b32_e32 v113, -16, v125
	v_cndmask_b32_e32 v110, v242, v110, vcc
	v_add_f32_e32 v111, v111, v112
	v_cmp_eq_u32_e32 vcc, s76, v113
	v_mov_b64_e32 v[126:127], v[78:79]
	v_mov_b64_e32 v[124:125], v[76:77]
	v_cndmask_b32_e32 v111, v242, v111, vcc
	v_mov_b64_e32 v[122:123], v[74:75]
	v_mov_b64_e32 v[120:121], v[72:73]
	v_mov_b64_e32 v[118:119], v[70:71]
	v_mov_b64_e32 v[116:117], v[68:69]
	v_mov_b64_e32 v[114:115], v[66:67]
	v_mov_b64_e32 v[112:113], v[64:65]

.LBB0_672:
	s_cmp_lt_u32 s50, 3
	s_cbranch_scc1 .LBB0_706
	s_add_i32 s6, s23, s90
	s_add_i32 s6, s6, -7
	s_cmp_gt_u32 s6, 7
	s_cselect_b64 vcc, -1, 0
	s_add_i32 s6, s23, s27
	s_max_i32 s6, s6, -7
	s_add_i32 s6, s6, 7
	s_min_u32 s6, s6, 14
	s_mulk_i32 s6, 0x7c
	v_add_u32_e32 v124, s6, v228
	v_mov_b32_e32 v122, v223
	ds_read_b32 v123, v124 offset:128
	ds_read_b32 v96, v124
	ds_read_b32 v97, v124 offset:4
	ds_read_b32 v98, v124 offset:8
	ds_read_b32 v99, v124 offset:12
	ds_read_b32 v100, v124 offset:32
	ds_read_b32 v101, v124 offset:36
	v_cndmask_b32_e32 v121, 0, v242, vcc
	v_cmp_gt_u32_e32 vcc, 16, v122
	s_waitcnt lgkmcnt(5)
	v_add_f32_e32 v96, v121, v96
	v_add_f32_e32 v96, v80, v96
	v_cndmask_b32_e32 v96, v242, v96, vcc
	ds_read_b32 v102, v124 offset:40
	ds_read_b32 v80, v124 offset:132
	v_add_u32_e32 v125, 1, v122
	v_cmp_gt_u32_e32 vcc, 16, v125
	s_waitcnt lgkmcnt(6)
	v_add_f32_e32 v97, v121, v97
	v_add_f32_e32 v97, v81, v97
	v_cndmask_b32_e32 v97, v242, v97, vcc
	ds_read_b32 v103, v124 offset:44
	ds_read_b32 v81, v124 offset:136
	v_add_u32_e32 v126, 2, v122
	v_cmp_gt_u32_e32 vcc, 16, v126
	s_waitcnt lgkmcnt(7)
	v_add_f32_e32 v98, v121, v98
	v_add_f32_e32 v98, v82, v98
	v_cndmask_b32_e32 v98, v242, v98, vcc
	ds_read_b32 v104, v124 offset:64
	ds_read_b32 v82, v124 offset:140
	v_add_u32_e32 v127, 3, v122
	v_cmp_gt_u32_e32 vcc, 16, v127
	s_waitcnt lgkmcnt(8)
	v_add_f32_e32 v99, v121, v99
	v_add_f32_e32 v99, v83, v99
	v_cndmask_b32_e32 v99, v242, v99, vcc
	ds_read_b32 v105, v124 offset:68
	ds_read_b32 v83, v124 offset:160
	v_add_u32_e32 v229, 8, v122
	v_cmp_gt_u32_e32 vcc, 16, v229
	s_waitcnt lgkmcnt(9)
	v_add_f32_e32 v100, v121, v100
	v_add_f32_e32 v100, v84, v100
	v_cndmask_b32_e32 v100, v242, v100, vcc
	ds_read_b32 v106, v124 offset:72
	ds_read_b32 v84, v124 offset:164
	v_add_u32_e32 v230, 9, v122
	v_cmp_gt_u32_e32 vcc, 16, v230
	s_waitcnt lgkmcnt(10)
	v_add_f32_e32 v101, v121, v101
	v_add_f32_e32 v101, v85, v101
	v_cndmask_b32_e32 v101, v242, v101, vcc
	ds_read_b32 v107, v124 offset:76
	ds_read_b32 v85, v124 offset:168
	v_add_u32_e32 v231, 10, v122
	v_cmp_gt_u32_e32 vcc, 16, v231
	s_waitcnt lgkmcnt(11)
	v_add_f32_e32 v102, v121, v102
	v_add_f32_e32 v102, v86, v102
	v_cndmask_b32_e32 v102, v242, v102, vcc
	ds_read_b32 v108, v124 offset:96
	ds_read_b32 v86, v124 offset:172
	v_add_u32_e32 v232, 11, v122
	v_cmp_gt_u32_e32 vcc, 16, v232
	s_waitcnt lgkmcnt(11)
	v_add_f32_e32 v103, v121, v103
	v_add_f32_e32 v103, v87, v103
	v_cndmask_b32_e32 v103, v242, v103, vcc
	ds_read_b32 v109, v124 offset:100
	ds_read_b32 v87, v124 offset:192
	v_cmp_lt_u32_e32 vcc, s79, v122
	s_waitcnt lgkmcnt(11)
	v_add_f32_e32 v104, v121, v104
	v_add_f32_e32 v104, v88, v104
	v_cndmask_b32_e32 v104, v242, v104, vcc
	ds_read_b32 v110, v124 offset:104
	ds_read_b32 v88, v124 offset:196
	v_add_u32_e32 v233, 17, v122
	v_cmp_gt_u32_e32 vcc, 16, v233
	s_waitcnt lgkmcnt(11)
	v_add_f32_e32 v105, v121, v105
	v_add_f32_e32 v105, v89, v105
	v_cndmask_b32_e32 v105, v242, v105, vcc
	ds_read_b32 v111, v124 offset:108
	ds_read_b32 v89, v124 offset:200
	v_add_u32_e32 v247, 18, v122
	v_cmp_gt_u32_e32 vcc, 16, v247
	s_waitcnt lgkmcnt(11)
	v_add_f32_e32 v106, v121, v106
	v_add_f32_e32 v106, v90, v106
	v_cndmask_b32_e32 v106, v242, v106, vcc
	ds_read_b32 v90, v124 offset:204
	v_add_u32_e32 v248, 19, v122
	v_cmp_gt_u32_e32 vcc, 16, v248
	s_waitcnt lgkmcnt(10)
	v_add_f32_e32 v107, v121, v107
	v_add_f32_e32 v107, v91, v107
	v_cndmask_b32_e32 v107, v242, v107, vcc
	ds_read_b32 v91, v124 offset:224
	v_add_u32_e32 v249, 24, v122
	v_cmp_gt_u32_e32 vcc, 16, v249
	s_waitcnt lgkmcnt(9)
	v_add_f32_e32 v108, v121, v108
	v_add_f32_e32 v108, v92, v108
	v_cndmask_b32_e32 v108, v242, v108, vcc
	ds_read_b32 v92, v124 offset:228
	v_add_u32_e32 v250, 25, v122
	v_cmp_gt_u32_e32 vcc, 16, v250
	s_waitcnt lgkmcnt(8)
	v_add_f32_e32 v109, v121, v109
	v_add_f32_e32 v109, v93, v109
	v_cndmask_b32_e32 v109, v242, v109, vcc
	ds_read_b32 v251, v124 offset:232
	v_add_u32_e32 v239, 26, v122
	v_cmp_gt_u32_e32 vcc, 16, v239
	s_waitcnt lgkmcnt(7)
	v_add_f32_e32 v110, v121, v110
	v_add_f32_e32 v110, v94, v110
	v_cndmask_b32_e32 v110, v242, v110, vcc
	ds_read_b32 v94, v124 offset:236
	v_add_u32_e32 v93, 27, v122
	v_cmp_gt_u32_e32 vcc, 16, v93
	s_waitcnt lgkmcnt(6)
	v_add_f32_e32 v111, v121, v111
	v_add_f32_e32 v111, v95, v111
	v_cndmask_b32_e32 v111, v242, v111, vcc
	s_waitcnt lgkmcnt(14)
	v_add_f32_e32 v95, v121, v123
	v_and_b32_e32 v122, -16, v122
	v_add_f32_e32 v64, v64, v95
	v_cmp_eq_u32_e32 vcc, s76, v122
	v_add_f32_e32 v80, v121, v80
	v_and_b32_e32 v95, -16, v125
	v_cndmask_b32_e32 v64, v242, v64, vcc
	v_add_f32_e32 v65, v65, v80
	v_cmp_eq_u32_e32 vcc, s76, v95
	s_waitcnt lgkmcnt(13)
	v_add_f32_e32 v80, v121, v81
	v_and_b32_e32 v81, -16, v126
	v_cndmask_b32_e32 v65, v242, v65, vcc
	v_add_f32_e32 v66, v66, v80
	v_cmp_eq_u32_e32 vcc, s76, v81
	s_waitcnt lgkmcnt(12)
	v_add_f32_e32 v80, v121, v82
	v_and_b32_e32 v81, -16, v127
	v_cndmask_b32_e32 v66, v242, v66, vcc
	v_add_f32_e32 v67, v67, v80
	v_cmp_eq_u32_e32 vcc, s76, v81
	s_waitcnt lgkmcnt(11)
	v_add_f32_e32 v80, v121, v83
	v_and_b32_e32 v81, -16, v229
	v_cndmask_b32_e32 v67, v242, v67, vcc
	v_add_f32_e32 v68, v68, v80
	v_cmp_eq_u32_e32 vcc, s76, v81
	s_waitcnt lgkmcnt(10)
	v_add_f32_e32 v80, v121, v84
	v_and_b32_e32 v81, -16, v230
	v_cndmask_b32_e32 v68, v242, v68, vcc
	v_add_f32_e32 v69, v69, v80
	v_cmp_eq_u32_e32 vcc, s76, v81
	s_waitcnt lgkmcnt(9)
	v_add_f32_e32 v80, v121, v85
	v_and_b32_e32 v81, -16, v231
	v_cndmask_b32_e32 v69, v242, v69, vcc
	v_add_f32_e32 v70, v70, v80
	v_cmp_eq_u32_e32 vcc, s76, v81
	s_waitcnt lgkmcnt(8)
	v_add_f32_e32 v80, v121, v86
	v_and_b32_e32 v81, -16, v232
	v_cndmask_b32_e32 v70, v242, v70, vcc
	v_add_f32_e32 v71, v71, v80
	v_cmp_eq_u32_e32 vcc, s76, v81
	s_waitcnt lgkmcnt(7)
	v_add_f32_e32 v80, v121, v87
	v_add_f32_e32 v72, v72, v80
	v_cndmask_b32_e32 v71, v242, v71, vcc
	v_cmp_eq_u32_e32 vcc, s78, v122
	s_waitcnt lgkmcnt(6)
	v_add_f32_e32 v80, v121, v88
	v_and_b32_e32 v81, -16, v233
	v_cndmask_b32_e32 v72, v242, v72, vcc
	v_add_f32_e32 v73, v73, v80
	v_cmp_eq_u32_e32 vcc, s76, v81
	s_waitcnt lgkmcnt(5)
	v_add_f32_e32 v80, v121, v89
	v_and_b32_e32 v81, -16, v247
	v_cndmask_b32_e32 v73, v242, v73, vcc
	v_add_f32_e32 v74, v74, v80
	v_cmp_eq_u32_e32 vcc, s76, v81
	s_waitcnt lgkmcnt(4)
	v_add_f32_e32 v80, v121, v90
	v_and_b32_e32 v81, -16, v248
	v_cndmask_b32_e32 v74, v242, v74, vcc
	v_add_f32_e32 v75, v75, v80
	v_cmp_eq_u32_e32 vcc, s76, v81
	s_waitcnt lgkmcnt(3)
	v_add_f32_e32 v80, v121, v91
	v_and_b32_e32 v81, -16, v249
	v_cndmask_b32_e32 v75, v242, v75, vcc
	v_add_f32_e32 v76, v76, v80
	v_cmp_eq_u32_e32 vcc, s76, v81
	s_waitcnt lgkmcnt(2)
	v_add_f32_e32 v80, v121, v92
	v_and_b32_e32 v81, -16, v250
	v_cndmask_b32_e32 v76, v242, v76, vcc
	v_add_f32_e32 v77, v77, v80
	v_cmp_eq_u32_e32 vcc, s76, v81
	s_waitcnt lgkmcnt(1)
	v_add_f32_e32 v80, v121, v251
	v_and_b32_e32 v81, -16, v239
	v_cndmask_b32_e32 v77, v242, v77, vcc
	v_add_f32_e32 v78, v78, v80
	v_cmp_eq_u32_e32 vcc, s76, v81
	s_waitcnt lgkmcnt(0)
	v_add_f32_e32 v80, v121, v94
	v_and_b32_e32 v81, -16, v93
	v_cndmask_b32_e32 v78, v242, v78, vcc
	v_add_f32_e32 v79, v79, v80
	v_cmp_eq_u32_e32 vcc, s76, v81
	v_mov_b64_e32 v[80:81], v[96:97]
	v_mov_b64_e32 v[82:83], v[98:99]
	v_cndmask_b32_e32 v79, v242, v79, vcc
	v_mov_b64_e32 v[84:85], v[100:101]
	v_mov_b64_e32 v[86:87], v[102:103]
	v_mov_b64_e32 v[88:89], v[104:105]
	v_mov_b64_e32 v[90:91], v[106:107]
	v_mov_b64_e32 v[92:93], v[108:109]
	v_mov_b64_e32 v[94:95], v[110:111]

.LBB0_737:
	v_add_u32_e32 v0, s81, v226
	ds_read_b64_tr_b16 v[6:7], v0 offset:24576
	ds_read_b64_tr_b16 v[8:9], v0 offset:25088
	s_waitcnt lgkmcnt(9)
	v_mfma_f32_32x32x16_bf16 v[96:111], v[188:191], v[156:159], v[48:63]
	v_add_f32_e32 v2, v80, v81
	v_add_f32_e32 v2, v82, v2
	v_add_f32_e32 v2, v83, v2
	v_add_f32_e32 v2, v84, v2
	v_add_f32_e32 v10, v85, v2
	v_cvt_pk_bf16_f32 v140, v80, v81
	v_cvt_pk_bf16_f32 v141, v82, v83
	ds_read_b64_tr_b16 v[2:3], v0 offset:28672
	ds_read_b64_tr_b16 v[4:5], v0 offset:29184
	s_waitcnt lgkmcnt(10)
	v_mfma_f32_32x32x16_bf16 v[48:63], v[184:187], v[156:159], v[48:63]
	v_add_f32_e32 v10, v86, v10
	v_add_f32_e32 v10, v87, v10
	v_add_f32_e32 v10, v88, v10
	v_add_f32_e32 v14, v89, v10
	v_cvt_pk_bf16_f32 v142, v84, v85
	v_cvt_pk_bf16_f32 v143, v86, v87
	ds_read_b64_tr_b16 v[10:11], v0 offset:25600
	ds_read_b64_tr_b16 v[12:13], v0 offset:26112
	s_waitcnt lgkmcnt(11)
	v_mfma_f32_32x32x16_bf16 v[96:111], v[180:183], v[152:155], v[96:111]
	v_add_f32_e32 v14, v90, v14
	v_add_f32_e32 v14, v91, v14
	v_add_f32_e32 v14, v92, v14
	v_add_f32_e32 v14, v93, v14
	v_cvt_pk_bf16_f32 v136, v88, v89
	v_cvt_pk_bf16_f32 v137, v90, v91
	ds_read_b64_tr_b16 v[80:81], v0 offset:29696
	ds_read_b64_tr_b16 v[82:83], v0 offset:30208
	s_waitcnt lgkmcnt(12)
	v_mfma_f32_32x32x16_bf16 v[48:63], v[176:179], v[152:155], v[48:63]
	v_add_f32_e32 v14, v94, v14
	v_add_f32_e32 v14, v95, v14
	v_add_f32_e32 v14, v64, v14
	v_add_f32_e32 v14, v65, v14
	v_cvt_pk_bf16_f32 v138, v92, v93
	v_cvt_pk_bf16_f32 v139, v94, v95
	ds_read_b64_tr_b16 v[84:85], v0 offset:26624
	ds_read_b64_tr_b16 v[86:87], v0 offset:27136
	s_waitcnt lgkmcnt(13)
	v_mfma_f32_32x32x16_bf16 v[96:111], v[172:175], v[148:151], v[96:111]
	v_add_f32_e32 v14, v66, v14
	v_add_f32_e32 v14, v67, v14
	v_add_f32_e32 v14, v68, v14
	v_add_f32_e32 v14, v69, v14
	v_cvt_pk_bf16_f32 v132, v64, v65
	v_cvt_pk_bf16_f32 v133, v66, v67
	ds_read_b64_tr_b16 v[88:89], v0 offset:30720
	ds_read_b64_tr_b16 v[90:91], v0 offset:31232
	s_waitcnt lgkmcnt(14)
	v_mfma_f32_32x32x16_bf16 v[48:63], v[168:171], v[148:151], v[48:63]
	v_add_f32_e32 v14, v70, v14
	v_add_f32_e32 v14, v71, v14
	v_add_f32_e32 v14, v72, v14
	v_add_f32_e32 v14, v73, v14
	v_cvt_pk_bf16_f32 v134, v68, v69
	v_cvt_pk_bf16_f32 v135, v70, v71
	ds_read_b64_tr_b16 v[92:93], v0 offset:27648
	ds_read_b64_tr_b16 v[94:95], v0 offset:28160
	s_waitcnt lgkmcnt(14)
	v_mfma_f32_32x32x16_bf16 v[96:111], v[164:167], v[144:147], v[96:111]
	v_add_f32_e32 v14, v74, v14
	v_add_f32_e32 v14, v75, v14
	v_add_f32_e32 v14, v76, v14
	v_add_f32_e32 v14, v77, v14
	v_cvt_pk_bf16_f32 v128, v72, v73
	v_cvt_pk_bf16_f32 v129, v74, v75
	ds_read_b64_tr_b16 v[112:113], v0 offset:31744
	ds_read_b64_tr_b16 v[114:115], v0 offset:32256
	v_mfma_f32_32x32x16_bf16 v[48:63], v[160:163], v[144:147], v[48:63]
	v_add_f32_e32 v0, v78, v14
	v_add_f32_e32 v0, v79, v0
	v_add_f32_e32 v0, 0, v0
	v_cvt_pk_bf16_f32 v130, v76, v77
	v_cvt_pk_bf16_f32 v131, v78, v79
	s_cmp_lt_i32 s0, 5
	s_cbranch_scc1 .LBB0_771
	s_add_i32 s65, s65, s63
	s_max_i32 s0, s65, 4
	s_add_i32 s0, s0, -4
	s_min_u32 s0, s0, 56
	s_add_i32 s13, s13, s12
	s_sub_i32 s0, s13, s0
	s_cmp_gt_u32 s0, 7
	s_cselect_b64 vcc, -1, 0
	s_sub_i32 s0, s13, s65
	s_max_i32 s0, s0, -7
	s_add_i32 s0, s0, 7
	s_min_u32 s0, s0, 14
	s_mulk_i32 s0, 0x7c
	v_lshlrev_b32_e32 v14, 2, v224
	v_add3_u32 v116, v225, s0, v14
	ds_read_b32 v15, v116 offset:128
	ds_read_b32 v64, v116
	ds_read_b32 v65, v116 offset:4
	ds_read_b32 v66, v116 offset:8
	ds_read_b32 v67, v116 offset:12
	ds_read_b32 v68, v116 offset:32
	ds_read_b32 v69, v116 offset:36
	v_cndmask_b32_e32 v14, 0, v242, vcc
	v_cmp_gt_u32_e32 vcc, 16, v223
	s_waitcnt lgkmcnt(5)
	v_add_f32_e32 v64, v14, v64
	v_add_f32_e32 v64, v96, v64
	v_cndmask_b32_e32 v64, v242, v64, vcc
	ds_read_b32 v70, v116 offset:40
	ds_read_b32 v96, v116 offset:132
	v_add_u32_e32 v117, 1, v223
	v_cmp_gt_u32_e32 vcc, 16, v117
	s_waitcnt lgkmcnt(6)
	v_add_f32_e32 v65, v14, v65
	v_add_f32_e32 v65, v97, v65
	v_cndmask_b32_e32 v65, v242, v65, vcc
	ds_read_b32 v71, v116 offset:44
	ds_read_b32 v97, v116 offset:136
	v_add_u32_e32 v118, 2, v223
	v_cmp_gt_u32_e32 vcc, 16, v118
	s_waitcnt lgkmcnt(7)
	v_add_f32_e32 v66, v14, v66
	v_add_f32_e32 v66, v98, v66
	v_cndmask_b32_e32 v66, v242, v66, vcc
	ds_read_b32 v72, v116 offset:64
	ds_read_b32 v98, v116 offset:140
	v_add_u32_e32 v119, 3, v223
	v_cmp_gt_u32_e32 vcc, 16, v119
	s_waitcnt lgkmcnt(8)
	v_add_f32_e32 v67, v14, v67
	v_add_f32_e32 v67, v99, v67
	v_cndmask_b32_e32 v67, v242, v67, vcc
	ds_read_b32 v73, v116 offset:68
	ds_read_b32 v99, v116 offset:160
	v_add_u32_e32 v120, 8, v223
	v_cmp_gt_u32_e32 vcc, 16, v120
	s_waitcnt lgkmcnt(9)
	v_add_f32_e32 v68, v14, v68
	v_add_f32_e32 v68, v100, v68
	v_cndmask_b32_e32 v68, v242, v68, vcc
	ds_read_b32 v74, v116 offset:72
	ds_read_b32 v100, v116 offset:164
	v_add_u32_e32 v121, 9, v223
	v_cmp_gt_u32_e32 vcc, 16, v121
	s_waitcnt lgkmcnt(10)
	v_add_f32_e32 v69, v14, v69
	v_add_f32_e32 v69, v101, v69
	v_cndmask_b32_e32 v69, v242, v69, vcc
	ds_read_b32 v75, v116 offset:76
	ds_read_b32 v101, v116 offset:168
	v_add_u32_e32 v122, 10, v223
	v_cmp_gt_u32_e32 vcc, 16, v122
	s_waitcnt lgkmcnt(11)
	v_add_f32_e32 v70, v14, v70
	v_add_f32_e32 v70, v102, v70
	v_cndmask_b32_e32 v70, v242, v70, vcc
	ds_read_b32 v76, v116 offset:96
	ds_read_b32 v102, v116 offset:172
	v_add_u32_e32 v123, 11, v223
	v_cmp_gt_u32_e32 vcc, 16, v123
	s_waitcnt lgkmcnt(11)
	v_add_f32_e32 v71, v14, v71
	v_add_f32_e32 v71, v103, v71
	v_cndmask_b32_e32 v71, v242, v71, vcc
	ds_read_b32 v77, v116 offset:100
	ds_read_b32 v103, v116 offset:192
	v_cmp_lt_u32_e32 vcc, s79, v223
	s_waitcnt lgkmcnt(11)
	v_add_f32_e32 v72, v14, v72
	v_add_f32_e32 v72, v104, v72
	v_cndmask_b32_e32 v72, v242, v72, vcc
	ds_read_b32 v78, v116 offset:104
	ds_read_b32 v104, v116 offset:196
	v_add_u32_e32 v124, 17, v223
	v_cmp_gt_u32_e32 vcc, 16, v124
	s_waitcnt lgkmcnt(11)
	v_add_f32_e32 v73, v14, v73
	v_add_f32_e32 v73, v105, v73
	v_cndmask_b32_e32 v73, v242, v73, vcc
	ds_read_b32 v79, v116 offset:108
	ds_read_b32 v105, v116 offset:200
	v_add_u32_e32 v125, 18, v223
	v_cmp_gt_u32_e32 vcc, 16, v125
	s_waitcnt lgkmcnt(11)
	v_add_f32_e32 v74, v14, v74
	v_add_f32_e32 v74, v106, v74
	v_cndmask_b32_e32 v74, v242, v74, vcc
	ds_read_b32 v106, v116 offset:204
	v_add_u32_e32 v126, 19, v223
	v_cmp_gt_u32_e32 vcc, 16, v126
	s_waitcnt lgkmcnt(10)
	v_add_f32_e32 v75, v14, v75
	v_add_f32_e32 v75, v107, v75
	v_cndmask_b32_e32 v75, v242, v75, vcc
	ds_read_b32 v107, v116 offset:224
	v_add_u32_e32 v127, 24, v223
	v_cmp_gt_u32_e32 vcc, 16, v127
	s_waitcnt lgkmcnt(9)
	v_add_f32_e32 v76, v14, v76
	v_add_f32_e32 v76, v108, v76
	v_cndmask_b32_e32 v76, v242, v76, vcc
	ds_read_b32 v108, v116 offset:228
	v_add_u32_e32 v144, 25, v223
	v_cmp_gt_u32_e32 vcc, 16, v144
	s_waitcnt lgkmcnt(8)
	v_add_f32_e32 v77, v14, v77
	v_add_f32_e32 v77, v109, v77
	v_cndmask_b32_e32 v77, v242, v77, vcc
	ds_read_b32 v145, v116 offset:232
	v_add_u32_e32 v146, 26, v223
	v_cmp_gt_u32_e32 vcc, 16, v146
	s_waitcnt lgkmcnt(7)
	v_add_f32_e32 v78, v14, v78
	v_add_f32_e32 v78, v110, v78
	v_cndmask_b32_e32 v78, v242, v78, vcc
	ds_read_b32 v110, v116 offset:236
	v_add_u32_e32 v109, 27, v223
	v_cmp_gt_u32_e32 vcc, 16, v109
	s_waitcnt lgkmcnt(6)
	v_add_f32_e32 v79, v14, v79
	v_add_f32_e32 v79, v111, v79
	v_cndmask_b32_e32 v79, v242, v79, vcc
	s_waitcnt lgkmcnt(14)
	v_add_f32_e32 v15, v14, v15
	v_and_b32_e32 v111, -16, v223
	v_add_f32_e32 v15, v48, v15
	v_cmp_eq_u32_e32 vcc, s76, v111
	s_nop 1
	v_cndmask_b32_e32 v48, v242, v15, vcc
	v_add_f32_e32 v15, v14, v96
	v_and_b32_e32 v96, -16, v117
	v_add_f32_e32 v15, v49, v15
	v_cmp_eq_u32_e32 vcc, s76, v96
	v_and_b32_e32 v96, -16, v118
	s_nop 0
	v_cndmask_b32_e32 v49, v242, v15, vcc
	s_waitcnt lgkmcnt(13)
	v_add_f32_e32 v15, v14, v97
	v_add_f32_e32 v15, v50, v15
	v_cmp_eq_u32_e32 vcc, s76, v96
	v_and_b32_e32 v96, -16, v119
	s_nop 0
	v_cndmask_b32_e32 v50, v242, v15, vcc
	s_waitcnt lgkmcnt(12)
	v_add_f32_e32 v15, v14, v98
	v_add_f32_e32 v15, v51, v15
	v_cmp_eq_u32_e32 vcc, s76, v96
	v_and_b32_e32 v96, -16, v120
	s_nop 0
	v_cndmask_b32_e32 v51, v242, v15, vcc
	s_waitcnt lgkmcnt(11)
	v_add_f32_e32 v15, v14, v99
	v_add_f32_e32 v15, v52, v15
	v_cmp_eq_u32_e32 vcc, s76, v96
	v_and_b32_e32 v96, -16, v121
	s_nop 0
	v_cndmask_b32_e32 v52, v242, v15, vcc
	s_waitcnt lgkmcnt(10)
	v_add_f32_e32 v15, v14, v100
	v_add_f32_e32 v15, v53, v15
	v_cmp_eq_u32_e32 vcc, s76, v96
	v_and_b32_e32 v96, -16, v122
	s_nop 0
	v_cndmask_b32_e32 v53, v242, v15, vcc
	s_waitcnt lgkmcnt(9)
	v_add_f32_e32 v15, v14, v101
	v_add_f32_e32 v15, v54, v15
	v_cmp_eq_u32_e32 vcc, s76, v96
	v_and_b32_e32 v96, -16, v123
	s_nop 0
	v_cndmask_b32_e32 v54, v242, v15, vcc
	s_waitcnt lgkmcnt(8)
	v_add_f32_e32 v15, v14, v102
	v_add_f32_e32 v15, v55, v15
	v_cmp_eq_u32_e32 vcc, s76, v96
	v_and_b32_e32 v96, -16, v124
	s_nop 0
	v_cndmask_b32_e32 v55, v242, v15, vcc
	s_waitcnt lgkmcnt(7)
	v_add_f32_e32 v15, v14, v103
	v_add_f32_e32 v15, v56, v15
	v_cmp_eq_u32_e32 vcc, s78, v111
	s_nop 1
	v_cndmask_b32_e32 v56, v242, v15, vcc
	s_waitcnt lgkmcnt(6)
	v_add_f32_e32 v15, v14, v104
	v_add_f32_e32 v15, v57, v15
	v_cmp_eq_u32_e32 vcc, s76, v96
	v_and_b32_e32 v96, -16, v125
	s_nop 0
	v_cndmask_b32_e32 v57, v242, v15, vcc
	s_waitcnt lgkmcnt(5)
	v_add_f32_e32 v15, v14, v105
	v_add_f32_e32 v15, v58, v15
	v_cmp_eq_u32_e32 vcc, s76, v96
	v_and_b32_e32 v96, -16, v126
	s_nop 0
	v_cndmask_b32_e32 v58, v242, v15, vcc
	s_waitcnt lgkmcnt(4)
	v_add_f32_e32 v15, v14, v106
	v_add_f32_e32 v15, v59, v15
	v_cmp_eq_u32_e32 vcc, s76, v96
	v_and_b32_e32 v96, -16, v127
	s_nop 0
	v_cndmask_b32_e32 v59, v242, v15, vcc
	s_waitcnt lgkmcnt(3)
	v_add_f32_e32 v15, v14, v107
	v_add_f32_e32 v15, v60, v15
	v_cmp_eq_u32_e32 vcc, s76, v96
	v_and_b32_e32 v96, -16, v144
	s_nop 0
	v_cndmask_b32_e32 v60, v242, v15, vcc
	s_waitcnt lgkmcnt(2)
	v_add_f32_e32 v15, v14, v108
	v_add_f32_e32 v15, v61, v15
	v_cmp_eq_u32_e32 vcc, s76, v96
	v_and_b32_e32 v96, -16, v146
	s_nop 0
	v_cndmask_b32_e32 v61, v242, v15, vcc
	s_waitcnt lgkmcnt(1)
	v_add_f32_e32 v15, v14, v145
	v_add_f32_e32 v15, v62, v15
	v_cmp_eq_u32_e32 vcc, s76, v96
	s_waitcnt lgkmcnt(0)
	v_add_f32_e32 v14, v14, v110
	v_add_f32_e32 v14, v63, v14
	v_cndmask_b32_e32 v62, v242, v15, vcc
	v_and_b32_e32 v15, -16, v109
	v_cmp_eq_u32_e32 vcc, s76, v15
	v_mov_b64_e32 v[110:111], v[78:79]
	v_mov_b64_e32 v[108:109], v[76:77]
	v_cndmask_b32_e32 v63, v242, v14, vcc
	v_mov_b64_e32 v[106:107], v[74:75]
	v_mov_b64_e32 v[104:105], v[72:73]
	v_mov_b64_e32 v[102:103], v[70:71]
	v_mov_b64_e32 v[100:101], v[68:69]
	v_mov_b64_e32 v[98:99], v[66:67]
	v_mov_b64_e32 v[96:97], v[64:65]
